# baseline (speedup 1.0000x reference)
_Z6k_gramILi0EEvPK15HIP_vector_typeIjLj4EEPyPf:
	s_load_dwordx4 s[8:11], s[0:1], 0x0
	s_load_dwordx2 s[4:5], s[0:1], 0x10
	s_lshl_b32 s0, s2, 2
	s_and_b32 s0, s0, 28
	s_ashr_i32 s1, s2, 6
	s_add_i32 s16, s0, s1
	v_readfirstlane_b32 s23, v0
	s_ashr_i32 s17, s16, 31
	s_lshr_b32 s21, s23, 6
	s_bfe_u32 s18, s23, 0x20006
	s_lshr_b32 s22, s2, 3
	s_bfe_u32 s20, s2, 0x30003
	s_lshl_b64 s[0:1], s[16:17], 20
	s_waitcnt lgkmcnt(0)
	s_add_u32 s12, s8, s0
	v_mov_b32_e32 v1, 0x20000
	s_addc_u32 s0, s9, s1
	s_lshl_b32 s1, s20, 2
	v_lshl_or_b32 v1, v0, 2, v1
	v_bfrev_b32_e32 v2, 1
	s_cmp_lt_u32 s20, 4
	ds_write_b32 v1, v2
	s_mov_b32 s24, 4
	s_mov_b32 s15, 0x20000
	s_and_b32 s13, s0, 0xffff
	s_mov_b32 s14, 0x100000
	v_lshlrev_b32_e32 v166, 4, v0
	s_lshl_b32 s25, s21, 10
	s_lshl_b32 s0, s20, 17
	s_mov_b32 m0, s25
	s_nop 0
	buffer_load_dwordx4 v166, s[12:15], s0 offen lds
	s_add_i32 s27, s25, 0x4000
	s_or_b32 s2, s0, 0x8000
	s_mov_b32 m0, s27
	s_nop 0
	buffer_load_dwordx4 v166, s[12:15], s2 offen lds
	s_add_i32 s34, s25, 0x10000
	s_or_b32 s2, s0, 0x10000
	s_mov_b32 m0, s34
	s_nop 0
	buffer_load_dwordx4 v166, s[12:15], s2 offen lds
	s_add_i32 s36, s25, 0x14000
	s_or_b32 s2, s0, 0x18000
	s_mov_b32 m0, s36
	s_nop 0
	buffer_load_dwordx4 v166, s[12:15], s2 offen lds
	s_add_i32 s26, s25, 0x2000
	s_or_b32 s2, s0, 0x2000
	s_mov_b32 m0, s26
	s_nop 0
	buffer_load_dwordx4 v166, s[12:15], s2 offen lds
	s_add_i32 s28, s25, 0x6000
	s_or_b32 s2, s0, 0xa000
	s_mov_b32 m0, s28
	s_nop 0
	buffer_load_dwordx4 v166, s[12:15], s2 offen lds
	s_add_i32 s35, s25, 0x12000
	s_or_b32 s2, s0, 0x12000
	s_mov_b32 m0, s35
	s_nop 0
	buffer_load_dwordx4 v166, s[12:15], s2 offen lds
	s_add_i32 s37, s25, 0x16000
	s_or_b32 s2, s0, 0x1a000
	s_mov_b32 m0, s37
	s_nop 0
	buffer_load_dwordx4 v166, s[12:15], s2 offen lds
	s_add_i32 s29, s25, 0x8000
	s_or_b32 s2, s0, 0x4000
	s_mov_b32 m0, s29
	s_nop 0
	buffer_load_dwordx4 v166, s[12:15], s2 offen lds
	s_add_i32 s31, s25, 0xc000
	s_or_b32 s2, s0, 0xc000
	s_mov_b32 m0, s31
	s_nop 0
	buffer_load_dwordx4 v166, s[12:15], s2 offen lds
	s_add_i32 s38, s25, 0x18000
	s_or_b32 s2, s0, 0x14000
	s_mov_b32 m0, s38
	s_nop 0
	buffer_load_dwordx4 v166, s[12:15], s2 offen lds
	s_add_i32 s40, s25, 0x1c000
	s_or_b32 s2, s0, 0x1c000
	s_mov_b32 m0, s40
	s_nop 0
	buffer_load_dwordx4 v166, s[12:15], s2 offen lds
	s_add_i32 s30, s25, 0xa000
	s_or_b32 s2, s0, 0x6000
	s_mov_b32 m0, s30
	s_nop 0
	buffer_load_dwordx4 v166, s[12:15], s2 offen lds
	s_add_i32 s33, s25, 0xe000
	s_or_b32 s2, s0, 0xe000
	s_mov_b32 m0, s33
	s_nop 0
	buffer_load_dwordx4 v166, s[12:15], s2 offen lds
	s_add_i32 s39, s25, 0x1a000
	s_or_b32 s2, s0, 0x16000
	s_mov_b32 m0, s39
	s_nop 0
	buffer_load_dwordx4 v166, s[12:15], s2 offen lds
	s_add_i32 s42, s25, 0x1e000
	s_or_b32 s2, s0, 0x1e000
	s_mov_b32 m0, s42
	s_nop 0
	buffer_load_dwordx4 v166, s[12:15], s2 offen lds
	s_lshl_b32 s0, s23, 9
	s_lshl_b32 s2, s23, 8
	v_and_b32_e32 v167, 15, v0
	v_bfe_u32 v160, v0, 4, 2
	s_and_b32 s0, s0, 0x10000
	s_and_b32 s2, s2, 0x4000
	v_lshlrev_b32_e32 v128, 9, v160
	v_lshlrev_b32_e32 v129, 4, v167
	s_or_b32 s0, s0, s2
	v_or3_b32 v124, s0, v128, v129
	s_waitcnt vmcnt(12)
	s_waitcnt lgkmcnt(0)
	s_barrier
	s_lshr_b32 s41, s23, 8
	s_lshl_b32 s0, s41, 14
	s_lshl_b32 s50, s24, 2
	v_or3_b32 v168, s0, v128, v129
	s_or_b32 s43, s18, s1
	s_lshl_b32 s0, s16, 10
	s_lshl_b32 s1, s43, 5
	ds_read_b128 v[128:131], v168
	ds_read_b128 v[132:135], v168 offset:256
	ds_read_b128 v[136:139], v168 offset:2048
	ds_read_b128 v[140:143], v168 offset:2304
	s_or_b32 s0, s1, s0
	v_or_b32_e32 v144, s0, v167
	v_lshlrev_b32_e32 v146, 2, v160
	v_ashrrev_i32_e32 v145, 31, v144
	v_lshl_add_u64 v[164:165], v[144:145], 2, s[4:5]
	v_or_b32_e32 v144, 1, v146
	v_cmp_eq_u32_e64 s[2:3], v144, v167
	v_or_b32_e32 v144, 2, v146
	v_cmp_eq_u32_e64 s[4:5], v144, v167
	v_or_b32_e32 v144, 3, v146
	s_add_i32 s44, s50, 3
	s_lshl_b32 s45, s22, 2
	v_cmp_eq_u32_e64 s[0:1], v146, v167
	v_cmp_eq_u32_e64 s[6:7], v144, v167
	v_add_u32_e32 v169, 0x10000, v168
	v_add_u32_e32 v170, 0x10100, v168
	v_add_u32_e32 v171, 0x10800, v168
	v_add_u32_e32 v172, 0x10900, v168
	s_and_b32 s8, s45, 28
	s_add_i32 s8, s8, s41
	s_lshl_b32 s19, s8, 1
	s_or_b32 s51, s19, 1
	v_mov_b32_e32 v234, s19
	v_mov_b32_e32 v235, s51
	s_and_b32 s46, s21, 3
	s_lshl_b32 s46, s46, 5
	v_lshl_or_b32 v173, v160, 3, s46
	s_lshl_b32 s47, s41, 7
	s_mov_b32 s48, 0
	s_movk_i32 s49, 0xffc0
	v_add_u32_e32 v174, 0x11000, v168
	v_add_u32_e32 v175, 0x11100, v168
	v_add_u32_e32 v176, 0x11800, v168
	v_add_u32_e32 v177, 0x11900, v168
	v_add_u32_e32 v178, 0x12000, v168
	v_add_u32_e32 v179, 0x12100, v168
	v_add_u32_e32 v180, 0x12800, v168
	v_add_u32_e32 v181, 0x12900, v168
	v_add_u32_e32 v182, 0x13000, v168
	v_add_u32_e32 v183, 0x13100, v168
	v_add_u32_e32 v184, 0x13800, v168
	v_add_u32_e32 v185, 0x13900, v168
	v_add_u32_e32 v186, 0x18000, v168
	v_add_u32_e32 v187, 0x18100, v168
	v_add_u32_e32 v188, 0x18800, v168
	v_add_u32_e32 v189, 0x18900, v168
	v_add_u32_e32 v190, 0x19000, v168
	v_add_u32_e32 v191, 0x19100, v168
	v_add_u32_e32 v192, 0x19800, v168
	v_add_u32_e32 v193, 0x19900, v168
	v_add_u32_e32 v194, 0x1a000, v168
	v_add_u32_e32 v195, 0x1a100, v168
	v_add_u32_e32 v196, 0x1a800, v168
	v_add_u32_e32 v197, 0x1a900, v168
	v_add_u32_e32 v198, 0x1b000, v168
	v_add_u32_e32 v199, 0x1b100, v168
	v_add_u32_e32 v200, 0x1b800, v168
	v_add_u32_e32 v201, 0x1b900, v168
	ds_read_b128 v[0:3], v124
	ds_read_b128 v[4:7], v124 offset:256
	ds_read_b128 v[8:11], v124 offset:2048
	ds_read_b128 v[12:15], v124 offset:2304
	ds_read_b128 v[144:147], v168
	ds_read_b128 v[148:151], v168 offset:256
	ds_read_b128 v[152:155], v168 offset:2048
	ds_read_b128 v[156:159], v168 offset:2304
	ds_read_b128 v[224:227], v168 offset:4096
	s_waitcnt lgkmcnt(4)
	v_mfma_f32_16x16x32_bf16 v[208:211], v[0:3], v[144:147], 0
	v_mfma_f32_16x16x32_bf16 v[212:215], v[4:7], v[144:147], 0
	ds_read_b128 v[228:231], v168 offset:4352
	ds_read_b128 v[16:19], v124 offset:4096
	ds_read_b128 v[20:23], v124 offset:4352
	s_waitcnt lgkmcnt(6)
	v_mfma_f32_16x16x32_bf16 v[216:219], v[0:3], v[148:151], 0
	v_mfma_f32_16x16x32_bf16 v[220:223], v[4:7], v[148:151], 0
	ds_read_b128 v[144:147], v168 offset:6144
	s_waitcnt lgkmcnt(6)
	v_mfma_f32_16x16x32_bf16 v[208:211], v[8:11], v[152:155], v[208:211]
	v_mfma_f32_16x16x32_bf16 v[212:215], v[12:15], v[152:155], v[212:215]
	ds_read_b128 v[148:151], v168 offset:6400
	ds_read_b128 v[24:27], v124 offset:6144
	ds_read_b128 v[28:31], v124 offset:6400
	s_waitcnt lgkmcnt(8)
	v_mfma_f32_16x16x32_bf16 v[216:219], v[8:11], v[156:159], v[216:219]
	v_mfma_f32_16x16x32_bf16 v[220:223], v[12:15], v[156:159], v[220:223]
	s_waitcnt lgkmcnt(4)
	v_mfma_f32_16x16x32_bf16 v[208:211], v[16:19], v[224:227], v[208:211]
	v_mfma_f32_16x16x32_bf16 v[212:215], v[20:23], v[224:227], v[212:215]
	v_mfma_f32_16x16x32_bf16 v[216:219], v[16:19], v[228:231], v[216:219]
	v_mfma_f32_16x16x32_bf16 v[220:223], v[20:23], v[228:231], v[220:223]
	s_waitcnt lgkmcnt(0)
	v_mfma_f32_16x16x32_bf16 v[208:211], v[24:27], v[144:147], v[208:211]
	v_mfma_f32_16x16x32_bf16 v[212:215], v[28:31], v[144:147], v[212:215]
	v_mfma_f32_16x16x32_bf16 v[216:219], v[24:27], v[148:151], v[216:219]
	v_mfma_f32_16x16x32_bf16 v[220:223], v[28:31], v[148:151], v[220:223]
	s_waitcnt vmcnt(8)
	s_barrier
	ds_read_b128 v[152:155], v168 offset:8192
	ds_read_b128 v[156:159], v168 offset:8448
	ds_read_b128 v[224:227], v168 offset:10240
	ds_read_b128 v[228:231], v168 offset:10496
	ds_read_b128 v[144:147], v168 offset:12288
	ds_read_b128 v[32:35], v124 offset:8192
	ds_read_b128 v[36:39], v124 offset:8448
	ds_read_b128 v[40:43], v124 offset:10240
	ds_read_b128 v[44:47], v124 offset:10496
	s_waitcnt lgkmcnt(2)
	v_mfma_f32_16x16x32_bf16 v[208:211], v[32:35], v[152:155], v[208:211]
	v_mfma_f32_16x16x32_bf16 v[212:215], v[36:39], v[152:155], v[212:215]
	ds_read_b128 v[148:151], v168 offset:12544
	ds_read_b128 v[48:51], v124 offset:12288
	ds_read_b128 v[52:55], v124 offset:12544
	v_mfma_f32_16x16x32_bf16 v[216:219], v[32:35], v[156:159], v[216:219]
	v_mfma_f32_16x16x32_bf16 v[220:223], v[36:39], v[156:159], v[220:223]
	ds_read_b128 v[152:155], v168 offset:14336
	s_waitcnt lgkmcnt(4)
	v_mfma_f32_16x16x32_bf16 v[208:211], v[40:43], v[224:227], v[208:211]
	v_mfma_f32_16x16x32_bf16 v[212:215], v[44:47], v[224:227], v[212:215]
	ds_read_b128 v[156:159], v168 offset:14592
	ds_read_b128 v[56:59], v124 offset:14336
	ds_read_b128 v[60:63], v124 offset:14592
	v_mfma_f32_16x16x32_bf16 v[216:219], v[40:43], v[228:231], v[216:219]
	v_mfma_f32_16x16x32_bf16 v[220:223], v[44:47], v[228:231], v[220:223]
	s_waitcnt lgkmcnt(4)
	v_mfma_f32_16x16x32_bf16 v[208:211], v[48:51], v[144:147], v[208:211]
	v_mfma_f32_16x16x32_bf16 v[212:215], v[52:55], v[144:147], v[212:215]
	v_mfma_f32_16x16x32_bf16 v[216:219], v[48:51], v[148:151], v[216:219]
	v_mfma_f32_16x16x32_bf16 v[220:223], v[52:55], v[148:151], v[220:223]
	s_waitcnt lgkmcnt(0)
	v_mfma_f32_16x16x32_bf16 v[208:211], v[56:59], v[152:155], v[208:211]
	v_mfma_f32_16x16x32_bf16 v[212:215], v[60:63], v[152:155], v[212:215]
	v_mfma_f32_16x16x32_bf16 v[216:219], v[56:59], v[156:159], v[216:219]
	v_mfma_f32_16x16x32_bf16 v[220:223], v[60:63], v[156:159], v[220:223]
	ds_read_b128 v[144:147], v169
	ds_read_b128 v[148:151], v169 offset:256
	ds_read_b128 v[152:155], v169 offset:2048
	ds_read_b128 v[156:159], v169 offset:2304
	ds_read_b128 v[224:227], v169 offset:4096
	s_waitcnt lgkmcnt(4)
	v_mfma_f32_16x16x32_bf16 v[136:139], v[0:3], v[144:147], 0
	v_mfma_f32_16x16x32_bf16 v[128:131], v[4:7], v[144:147], 0
	ds_read_b128 v[228:231], v169 offset:4352
	s_waitcnt lgkmcnt(4)
	v_mfma_f32_16x16x32_bf16 v[140:143], v[0:3], v[148:151], 0
	v_mfma_f32_16x16x32_bf16 v[132:135], v[4:7], v[148:151], 0
	ds_read_b128 v[144:147], v169 offset:6144
	s_waitcnt lgkmcnt(4)
	v_mfma_f32_16x16x32_bf16 v[136:139], v[8:11], v[152:155], v[136:139]
	v_mfma_f32_16x16x32_bf16 v[128:131], v[12:15], v[152:155], v[128:131]
	ds_read_b128 v[148:151], v169 offset:6400
	s_waitcnt lgkmcnt(4)
	v_mfma_f32_16x16x32_bf16 v[140:143], v[8:11], v[156:159], v[140:143]
	v_mfma_f32_16x16x32_bf16 v[132:135], v[12:15], v[156:159], v[132:135]
	s_waitcnt lgkmcnt(3)
	v_mfma_f32_16x16x32_bf16 v[136:139], v[16:19], v[224:227], v[136:139]
	v_mfma_f32_16x16x32_bf16 v[128:131], v[20:23], v[224:227], v[128:131]
	s_waitcnt lgkmcnt(2)
	v_mfma_f32_16x16x32_bf16 v[140:143], v[16:19], v[228:231], v[140:143]
	v_mfma_f32_16x16x32_bf16 v[132:135], v[20:23], v[228:231], v[132:135]
	s_waitcnt lgkmcnt(1)
	v_mfma_f32_16x16x32_bf16 v[136:139], v[24:27], v[144:147], v[136:139]
	v_mfma_f32_16x16x32_bf16 v[128:131], v[28:31], v[144:147], v[128:131]
	s_waitcnt lgkmcnt(0)
	v_mfma_f32_16x16x32_bf16 v[140:143], v[24:27], v[148:151], v[140:143]
	v_mfma_f32_16x16x32_bf16 v[132:135], v[28:31], v[148:151], v[132:135]
	s_waitcnt vmcnt(4)
	s_barrier
	s_add_i32 s60, s45, 4
	s_and_b32 s60, s60, 28
	s_lshl_b32 s60, s60, 15
	ds_read_b128 v[152:155], v169 offset:8192
	ds_read_b128 v[156:159], v169 offset:8448
	ds_read_b128 v[224:227], v169 offset:10240
	ds_read_b128 v[228:231], v169 offset:10496
	ds_read_b128 v[144:147], v169 offset:12288
	s_waitcnt lgkmcnt(4)
	v_mfma_f32_16x16x32_bf16 v[136:139], v[32:35], v[152:155], v[136:139]
	v_mfma_f32_16x16x32_bf16 v[128:131], v[36:39], v[152:155], v[128:131]
	ds_read_b128 v[148:151], v169 offset:12544
	ds_read_b128 v[64:67], v124 offset:32768
	ds_read_b128 v[68:71], v124 offset:33024
	s_waitcnt lgkmcnt(6)
	v_mfma_f32_16x16x32_bf16 v[140:143], v[32:35], v[156:159], v[140:143]
	s_mov_b32 s61, s60
	s_mov_b32 m0, s25
	s_nop 0
	buffer_load_dwordx4 v166, s[12:15], s61 offen lds
	v_mfma_f32_16x16x32_bf16 v[132:135], v[36:39], v[156:159], v[132:135]
	ds_read_b128 v[152:155], v169 offset:14336
	s_waitcnt lgkmcnt(6)
	v_mfma_f32_16x16x32_bf16 v[136:139], v[40:43], v[224:227], v[136:139]
	v_mfma_f32_16x16x32_bf16 v[128:131], v[44:47], v[224:227], v[128:131]
	ds_read_b128 v[156:159], v169 offset:14592
	ds_read_b128 v[72:75], v124 offset:34816
	ds_read_b128 v[76:79], v124 offset:35072
	s_waitcnt lgkmcnt(8)
	v_mfma_f32_16x16x32_bf16 v[140:143], v[40:43], v[228:231], v[140:143]
	s_or_b32 s61, s60, 0x2000
	s_mov_b32 m0, s26
	s_nop 0
	buffer_load_dwordx4 v166, s[12:15], s61 offen lds
	v_mfma_f32_16x16x32_bf16 v[132:135], v[44:47], v[228:231], v[132:135]
	s_waitcnt lgkmcnt(7)
	v_mfma_f32_16x16x32_bf16 v[136:139], v[48:51], v[144:147], v[136:139]
	v_mfma_f32_16x16x32_bf16 v[128:131], v[52:55], v[144:147], v[128:131]
	ds_read_b128 v[80:83], v124 offset:36864
	ds_read_b128 v[84:87], v124 offset:37120
	s_waitcnt lgkmcnt(8)
	v_mfma_f32_16x16x32_bf16 v[140:143], v[48:51], v[148:151], v[140:143]
	s_or_b32 s61, s60, 0x8000
	s_mov_b32 m0, s27
	s_nop 0
	buffer_load_dwordx4 v166, s[12:15], s61 offen lds
	v_mfma_f32_16x16x32_bf16 v[132:135], v[52:55], v[148:151], v[132:135]
	s_waitcnt lgkmcnt(5)
	v_mfma_f32_16x16x32_bf16 v[136:139], v[56:59], v[152:155], v[136:139]
	v_mfma_f32_16x16x32_bf16 v[128:131], v[60:63], v[152:155], v[128:131]
	ds_read_b128 v[88:91], v124 offset:38912
	ds_read_b128 v[92:95], v124 offset:39168
	s_waitcnt lgkmcnt(6)
	v_mfma_f32_16x16x32_bf16 v[140:143], v[56:59], v[156:159], v[140:143]
	s_or_b32 s61, s60, 0xa000
	s_mov_b32 m0, s28
	s_nop 0
	buffer_load_dwordx4 v166, s[12:15], s61 offen lds
	v_mfma_f32_16x16x32_bf16 v[132:135], v[60:63], v[156:159], v[132:135]
	s_barrier
	s_add_i32 s60, s45, 4
	s_and_b32 s60, s60, 28
	s_or_b32 s60, s60, 2
	s_lshl_b32 s60, s60, 15
	ds_read_b128 v[144:147], v168 offset:32768
	ds_read_b128 v[148:151], v168 offset:33024
	ds_read_b128 v[152:155], v168 offset:34816
	ds_read_b128 v[156:159], v168 offset:35072
	ds_read_b128 v[224:227], v168 offset:36864
	s_waitcnt lgkmcnt(4)
	v_mfma_f32_16x16x32_bf16 v[208:211], v[64:67], v[144:147], v[208:211]
	v_mfma_f32_16x16x32_bf16 v[212:215], v[68:71], v[144:147], v[212:215]
	ds_read_b128 v[228:231], v168 offset:37120
	s_waitcnt lgkmcnt(4)
	v_mfma_f32_16x16x32_bf16 v[216:219], v[64:67], v[148:151], v[216:219]
	s_mov_b32 s61, s60
	s_mov_b32 m0, s34
	s_nop 0
	buffer_load_dwordx4 v166, s[12:15], s61 offen lds
	v_mfma_f32_16x16x32_bf16 v[220:223], v[68:71], v[148:151], v[220:223]
	ds_read_b128 v[144:147], v168 offset:38912
	s_waitcnt lgkmcnt(4)
	v_mfma_f32_16x16x32_bf16 v[208:211], v[72:75], v[152:155], v[208:211]
	v_mfma_f32_16x16x32_bf16 v[212:215], v[76:79], v[152:155], v[212:215]
	ds_read_b128 v[148:151], v168 offset:39168
	s_waitcnt lgkmcnt(4)
	v_mfma_f32_16x16x32_bf16 v[216:219], v[72:75], v[156:159], v[216:219]
	v_mfma_f32_16x16x32_bf16 v[220:223], v[76:79], v[156:159], v[220:223]
	s_waitcnt lgkmcnt(3)
	v_mfma_f32_16x16x32_bf16 v[208:211], v[80:83], v[224:227], v[208:211]
	v_mfma_f32_16x16x32_bf16 v[212:215], v[84:87], v[224:227], v[212:215]
	s_waitcnt lgkmcnt(2)
	v_mfma_f32_16x16x32_bf16 v[216:219], v[80:83], v[228:231], v[216:219]
	s_or_b32 s61, s60, 0x2000
	s_mov_b32 m0, s35
	s_nop 0
	buffer_load_dwordx4 v166, s[12:15], s61 offen lds
	v_mfma_f32_16x16x32_bf16 v[220:223], v[84:87], v[228:231], v[220:223]
	s_waitcnt lgkmcnt(1)
	v_mfma_f32_16x16x32_bf16 v[208:211], v[88:91], v[144:147], v[208:211]
	v_mfma_f32_16x16x32_bf16 v[212:215], v[92:95], v[144:147], v[212:215]
	s_waitcnt lgkmcnt(0)
	v_mfma_f32_16x16x32_bf16 v[216:219], v[88:91], v[148:151], v[216:219]
	v_mfma_f32_16x16x32_bf16 v[220:223], v[92:95], v[148:151], v[220:223]
	ds_read_b128 v[144:147], v169 offset:32768
	ds_read_b128 v[148:151], v169 offset:33024
	ds_read_b128 v[152:155], v169 offset:34816
	ds_read_b128 v[156:159], v169 offset:35072
	ds_read_b128 v[224:227], v169 offset:36864
	s_waitcnt lgkmcnt(4)
	v_mfma_f32_16x16x32_bf16 v[136:139], v[64:67], v[144:147], v[136:139]
	v_mfma_f32_16x16x32_bf16 v[128:131], v[68:71], v[144:147], v[128:131]
	ds_read_b128 v[228:231], v169 offset:37120
	s_waitcnt lgkmcnt(4)
	v_mfma_f32_16x16x32_bf16 v[140:143], v[64:67], v[148:151], v[140:143]
	s_or_b32 s61, s60, 0x8000
	s_mov_b32 m0, s36
	s_nop 0
	buffer_load_dwordx4 v166, s[12:15], s61 offen lds
	v_mfma_f32_16x16x32_bf16 v[132:135], v[68:71], v[148:151], v[132:135]
	ds_read_b128 v[144:147], v169 offset:38912
	s_waitcnt lgkmcnt(4)
	v_mfma_f32_16x16x32_bf16 v[136:139], v[72:75], v[152:155], v[136:139]
	v_mfma_f32_16x16x32_bf16 v[128:131], v[76:79], v[152:155], v[128:131]
	ds_read_b128 v[148:151], v169 offset:39168
	s_waitcnt lgkmcnt(4)
	v_mfma_f32_16x16x32_bf16 v[140:143], v[72:75], v[156:159], v[140:143]
	v_mfma_f32_16x16x32_bf16 v[132:135], v[76:79], v[156:159], v[132:135]
	s_waitcnt lgkmcnt(3)
	v_mfma_f32_16x16x32_bf16 v[136:139], v[80:83], v[224:227], v[136:139]
	v_mfma_f32_16x16x32_bf16 v[128:131], v[84:87], v[224:227], v[128:131]
	s_waitcnt lgkmcnt(2)
	v_mfma_f32_16x16x32_bf16 v[140:143], v[80:83], v[228:231], v[140:143]
	s_or_b32 s61, s60, 0xa000
	s_mov_b32 m0, s37
	s_nop 0
	buffer_load_dwordx4 v166, s[12:15], s61 offen lds
	v_mfma_f32_16x16x32_bf16 v[132:135], v[84:87], v[228:231], v[132:135]
	s_waitcnt lgkmcnt(1)
	v_mfma_f32_16x16x32_bf16 v[136:139], v[88:91], v[144:147], v[136:139]
	v_mfma_f32_16x16x32_bf16 v[128:131], v[92:95], v[144:147], v[128:131]
	s_waitcnt lgkmcnt(0)
	v_mfma_f32_16x16x32_bf16 v[140:143], v[88:91], v[148:151], v[140:143]
	v_mfma_f32_16x16x32_bf16 v[132:135], v[92:95], v[148:151], v[132:135]
	s_waitcnt vmcnt(8)
	s_barrier
	ds_read_b128 v[152:155], v168 offset:40960
	ds_read_b128 v[156:159], v168 offset:41216
	ds_read_b128 v[224:227], v168 offset:43008
	ds_read_b128 v[228:231], v168 offset:43264
	ds_read_b128 v[144:147], v168 offset:45056
	ds_read_b128 v[96:99], v124 offset:40960
	ds_read_b128 v[100:103], v124 offset:41216
	ds_read_b128 v[104:107], v124 offset:43008
	ds_read_b128 v[108:111], v124 offset:43264
	s_waitcnt lgkmcnt(2)
	v_mfma_f32_16x16x32_bf16 v[208:211], v[96:99], v[152:155], v[208:211]
	v_mfma_f32_16x16x32_bf16 v[212:215], v[100:103], v[152:155], v[212:215]
	ds_read_b128 v[148:151], v168 offset:45312
	ds_read_b128 v[112:115], v124 offset:45056
	ds_read_b128 v[116:119], v124 offset:45312
	v_mfma_f32_16x16x32_bf16 v[216:219], v[96:99], v[156:159], v[216:219]
	v_mfma_f32_16x16x32_bf16 v[220:223], v[100:103], v[156:159], v[220:223]
	ds_read_b128 v[152:155], v168 offset:47104
	s_waitcnt lgkmcnt(4)
	v_mfma_f32_16x16x32_bf16 v[208:211], v[104:107], v[224:227], v[208:211]
	v_mfma_f32_16x16x32_bf16 v[212:215], v[108:111], v[224:227], v[212:215]
	ds_read_b128 v[156:159], v168 offset:47360
	ds_read_b128 v[120:123], v124 offset:47104
	ds_read_b128 v[124:127], v124 offset:47360
	v_mfma_f32_16x16x32_bf16 v[216:219], v[104:107], v[228:231], v[216:219]
	v_mfma_f32_16x16x32_bf16 v[220:223], v[108:111], v[228:231], v[220:223]
	s_waitcnt lgkmcnt(4)
	v_mfma_f32_16x16x32_bf16 v[208:211], v[112:115], v[144:147], v[208:211]
	v_mfma_f32_16x16x32_bf16 v[212:215], v[116:119], v[144:147], v[212:215]
	v_mfma_f32_16x16x32_bf16 v[216:219], v[112:115], v[148:151], v[216:219]
	v_mfma_f32_16x16x32_bf16 v[220:223], v[116:119], v[148:151], v[220:223]
	s_waitcnt lgkmcnt(0)
	v_mfma_f32_16x16x32_bf16 v[208:211], v[120:123], v[152:155], v[208:211]
	v_mfma_f32_16x16x32_bf16 v[212:215], v[124:127], v[152:155], v[212:215]
	v_mfma_f32_16x16x32_bf16 v[216:219], v[120:123], v[156:159], v[216:219]
	v_mfma_f32_16x16x32_bf16 v[220:223], v[124:127], v[156:159], v[220:223]
	s_waitcnt vmcnt(4)
	s_barrier
	s_nop 7
	s_nop 3
	s_cmp_lg_u32 s8, s43
	s_cbranch_scc1 .Ldiag0_done
	s_mov_b64 s[56:57], exec
	s_and_b64 exec, s[56:57], s[0:1]
	global_store_dword v[164:165], v208, off
	v_mov_b32_e32 v208, -1.0
	global_store_dword v[164:165], v220, off offset:64
	v_mov_b32_e32 v220, -1.0
	s_and_b64 exec, s[56:57], s[2:3]
	global_store_dword v[164:165], v209, off
	v_mov_b32_e32 v209, -1.0
	global_store_dword v[164:165], v221, off offset:64
	v_mov_b32_e32 v221, -1.0
	s_and_b64 exec, s[56:57], s[4:5]
	global_store_dword v[164:165], v210, off
	v_mov_b32_e32 v210, -1.0
	global_store_dword v[164:165], v222, off offset:64
	v_mov_b32_e32 v222, -1.0
	s_and_b64 exec, s[56:57], s[6:7]
	global_store_dword v[164:165], v211, off
	v_mov_b32_e32 v211, -1.0
	global_store_dword v[164:165], v223, off offset:64
	v_mov_b32_e32 v223, -1.0
	s_mov_b64 exec, s[56:57]
.Ldiag0_done:
	s_add_i32 s60, s45, 4
	s_and_b32 s60, s60, 28
	s_lshl_b32 s60, s60, 15
	ds_read_b128 v[152:155], v169 offset:40960
	ds_read_b128 v[156:159], v169 offset:41216
	ds_read_b128 v[224:227], v169 offset:43008
	ds_read_b128 v[228:231], v169 offset:43264
	ds_read_b128 v[144:147], v169 offset:45056
	s_waitcnt lgkmcnt(4)
	v_mfma_f32_16x16x32_bf16 v[136:139], v[96:99], v[152:155], v[136:139]
	v_mfma_f32_16x16x32_bf16 v[128:131], v[100:103], v[152:155], v[128:131]
	ds_read_b128 v[148:151], v169 offset:45312
	v_and_or_b32 v237, v208, s49, v234
	v_and_or_b32 v238, v216, s49, v235
	v_max_f32_e32 v161, v237, v238
	s_waitcnt lgkmcnt(4)
	v_mfma_f32_16x16x32_bf16 v[140:143], v[96:99], v[156:159], v[140:143]
	s_or_b32 s61, s60, 0x4000
	s_mov_b32 m0, s29
	s_nop 0
	buffer_load_dwordx4 v166, s[12:15], s61 offen lds
	v_mfma_f32_16x16x32_bf16 v[132:135], v[100:103], v[156:159], v[132:135]
	ds_read_b128 v[152:155], v169 offset:47104
	v_and_or_b32 v237, v209, s49, v234
	v_and_or_b32 v238, v217, s49, v235
	v_max_f32_e32 v160, v237, v238
	s_waitcnt lgkmcnt(4)
	v_mfma_f32_16x16x32_bf16 v[136:139], v[104:107], v[224:227], v[136:139]
	v_mfma_f32_16x16x32_bf16 v[128:131], v[108:111], v[224:227], v[128:131]
	ds_read_b128 v[156:159], v169 offset:47360
	v_and_or_b32 v237, v210, s49, v234
	v_and_or_b32 v238, v218, s49, v235
	v_max_f32_e32 v162, v237, v238
	s_waitcnt lgkmcnt(4)
	v_mfma_f32_16x16x32_bf16 v[140:143], v[104:107], v[228:231], v[140:143]
	s_or_b32 s61, s60, 0x6000
	s_mov_b32 m0, s30
	s_nop 0
	buffer_load_dwordx4 v166, s[12:15], s61 offen lds
	v_mfma_f32_16x16x32_bf16 v[132:135], v[108:111], v[228:231], v[132:135]
	v_and_or_b32 v237, v211, s49, v234
	v_and_or_b32 v238, v219, s49, v235
	v_max_f32_e32 v163, v237, v238
	s_waitcnt lgkmcnt(3)
	v_mfma_f32_16x16x32_bf16 v[136:139], v[112:115], v[144:147], v[136:139]
	v_mfma_f32_16x16x32_bf16 v[128:131], v[116:119], v[144:147], v[128:131]
	v_and_or_b32 v237, v212, s49, v234
	v_and_or_b32 v238, v220, s49, v235
	v_max_f32_e32 v203, v237, v238
	s_waitcnt lgkmcnt(2)
	v_mfma_f32_16x16x32_bf16 v[140:143], v[112:115], v[148:151], v[140:143]
	s_or_b32 s61, s60, 0xc000
	s_mov_b32 m0, s31
	s_nop 0
	buffer_load_dwordx4 v166, s[12:15], s61 offen lds
	v_mfma_f32_16x16x32_bf16 v[132:135], v[116:119], v[148:151], v[132:135]
	v_and_or_b32 v237, v213, s49, v234
	v_and_or_b32 v238, v221, s49, v235
	v_max_f32_e32 v204, v237, v238
	s_waitcnt lgkmcnt(1)
	v_mfma_f32_16x16x32_bf16 v[136:139], v[120:123], v[152:155], v[136:139]
	v_mfma_f32_16x16x32_bf16 v[128:131], v[124:127], v[152:155], v[128:131]
	v_and_or_b32 v237, v214, s49, v234
	v_and_or_b32 v238, v222, s49, v235
	v_max_f32_e32 v205, v237, v238
	s_waitcnt lgkmcnt(0)
	v_mfma_f32_16x16x32_bf16 v[140:143], v[120:123], v[156:159], v[140:143]
	s_or_b32 s61, s60, 0xe000
	s_mov_b32 m0, s33
	s_nop 0
	buffer_load_dwordx4 v166, s[12:15], s61 offen lds
	v_mfma_f32_16x16x32_bf16 v[132:135], v[124:127], v[156:159], v[132:135]
	v_and_or_b32 v237, v215, s49, v234
	v_and_or_b32 v238, v223, s49, v235
	v_max_f32_e32 v206, v237, v238
	v_lshl_or_b32 v202, v167, 2, s47
	v_add_u32_e32 v202, 0x1ff00, v202
	s_add_i32 s50, s50, -4
	s_mov_b32 s51, -1.0
	s_movk_i32 s52, 0xff80
	s_brev_b32 s53, -2
	ds_read_b128 v[144:147], v168
	ds_read_b128 v[148:151], v168 offset:256
	ds_read_b128 v[152:155], v168 offset:2048
	ds_read_b128 v[156:159], v168 offset:2304
	s_waitcnt vmcnt(0)
	s_branch .LBB3_13
